# speedup vs baseline: 1.0333x; 1.0333x over previous
.LBB4_7:
	v_mul_u32_u24_e32 v1, 0xa0, v1
	v_lshl_or_b32 v82, v96, 6, v98
	v_lshl_or_b32 v1, v97, 3, v1
	s_movk_i32 s4, 0x150
	v_mad_u32_u24 v1, v82, s4, v1
	v_cvt_pk_f16_f32 v37, v36, v37
	v_cvt_pk_f16_f32 v36, v34, v35
	v_cvt_pk_f16_f32 v35, v80, v81
	v_cvt_pk_f16_f32 v34, v78, v79
	s_waitcnt vmcnt(0)
	s_waitcnt vmcnt(0) lgkmcnt(0)
	s_barrier
	ds_write2_b64 v1, v[36:37], v[34:35] offset1:4
	v_cvt_pk_f16_f32 v35, v76, v77
	v_cvt_pk_f16_f32 v34, v74, v75
	v_cvt_pk_f16_f32 v37, v72, v73
	v_cvt_pk_f16_f32 v36, v70, v71
	ds_write2_b64 v1, v[34:35], v[36:37] offset0:8 offset1:12
	v_cvt_pk_f16_f32 v35, v64, v65
	v_cvt_pk_f16_f32 v34, v62, v63
	ds_write_b64 v1, v[34:35] offset:128
	v_cvt_pk_f16_f32 v35, v60, v61
	v_cvt_pk_f16_f32 v34, v58, v59
	v_cvt_pk_f16_f32 v37, v56, v57
	v_cvt_pk_f16_f32 v36, v54, v55
	v_add_u32_e32 v54, 0x1000, v1
	ds_write2_b64 v54, v[34:35], v[36:37] offset0:160 offset1:164
	v_cvt_pk_f16_f32 v35, v52, v53
	v_cvt_pk_f16_f32 v34, v50, v51
	v_cvt_pk_f16_f32 v37, v48, v49
	v_cvt_pk_f16_f32 v36, v46, v47
	v_cvt_pk_f16_f32 v13, v12, v13
	v_cvt_pk_f16_f32 v12, v10, v11
	v_add_u32_e32 v10, 0x3800, v1
	v_cvt_pk_f16_f32 v5, v4, v5
	v_cvt_pk_f16_f32 v4, v2, v3
	v_cvt_pk_f16_f32 v3, v8, v9
	v_cvt_pk_f16_f32 v2, v6, v7
	ds_write2_b64 v54, v[34:35], v[36:37] offset0:168 offset1:172
	v_cvt_pk_f16_f32 v35, v44, v45
	v_cvt_pk_f16_f32 v34, v42, v43
	v_cvt_pk_f16_f32 v21, v20, v21
	v_cvt_pk_f16_f32 v20, v18, v19
	ds_write2_b64 v10, v[4:5], v[2:3] offset0:232 offset1:236
	v_cvt_pk_f16_f32 v3, v68, v69
	v_cvt_pk_f16_f32 v2, v66, v67
	s_mov_b32 s6, 0xccccccd
	ds_write_b64 v1, v[34:35] offset:5504
	v_cvt_pk_f16_f32 v33, v32, v33
	v_cvt_pk_f16_f32 v32, v30, v31
	v_add_u32_e32 v30, 0x2800, v1
	ds_write_b64 v1, v[20:21] offset:10880
	ds_write_b64 v1, v[2:3] offset:16256
	v_mul_hi_u32 v1, v0, s6
	v_mul_u32_u24_e32 v2, 20, v1
	v_cvt_pk_f16_f32 v17, v16, v17
	v_cvt_pk_f16_f32 v16, v14, v15
	s_mov_b32 s3, 0
	v_sub_u32_e32 v2, v0, v2
	ds_write2_b64 v10, v[16:17], v[12:13] offset0:224 offset1:228
	s_lshl_b64 s[2:3], s[2:3], 1
	v_lshlrev_b32_e32 v10, 4, v2
	s_add_u32 s0, s0, s2
	v_mad_u32_u24 v2, v1, s4, v10
	v_or_b32_e32 v1, s10, v1
	s_addc_u32 s1, s1, s3
	v_mad_i64_i32 v[6:7], s[2:3], v1, s5, 0
	v_or_b32_e32 v1, 0x200, v0
	v_lshl_add_u64 v[6:7], v[6:7], 1, s[0:1]
	v_mov_b32_e32 v11, 0
	v_mul_hi_u32 v14, v1, s6
	v_cvt_pk_f16_f32 v35, v40, v41
	v_cvt_pk_f16_f32 v34, v38, v39
	v_cvt_pk_f16_f32 v29, v28, v29
	v_cvt_pk_f16_f32 v28, v26, v27
	v_cvt_pk_f16_f32 v25, v24, v25
	v_cvt_pk_f16_f32 v24, v22, v23
	v_lshl_add_u64 v[12:13], v[6:7], 0, v[10:11]
	v_mul_u32_u24_e32 v6, 20, v14
	ds_write2_b64 v30, v[34:35], v[32:33] offset0:64 offset1:68
	ds_write2_b64 v30, v[28:29], v[24:25] offset0:72 offset1:76
	s_waitcnt lgkmcnt(0)
	s_barrier
	ds_read_b128 v[2:5], v2
	v_sub_u32_e32 v1, v1, v6
	v_lshlrev_b32_e32 v10, 4, v1
	v_mad_u32_u24 v1, v14, s4, v10
	ds_read_b128 v[6:9], v1
	v_or_b32_e32 v1, s10, v14
	s_waitcnt lgkmcnt(1)
	global_store_dwordx4 v[12:13], v[2:5], off
	s_nop 1
	v_mad_i64_i32 v[2:3], s[2:3], v1, s5, 0
	v_lshl_add_u64 v[2:3], v[2:3], 1, s[0:1]
	v_lshl_add_u64 v[2:3], v[2:3], 0, v[10:11]
	v_or_b32_e32 v1, 0x400, v0
	s_waitcnt lgkmcnt(0)
	global_store_dwordx4 v[2:3], v[6:9], off
	s_nop 1
	v_mul_hi_u32 v6, v1, s6
	v_mul_u32_u24_e32 v2, 20, v6
	v_sub_u32_e32 v1, v1, v2
	v_lshlrev_b32_e32 v10, 4, v1
	v_mad_u32_u24 v1, v6, s4, v10
	ds_read_b128 v[2:5], v1
	v_or_b32_e32 v1, s10, v6
	v_mad_i64_i32 v[6:7], s[2:3], v1, s5, 0
	v_or_b32_e32 v1, 0x600, v0
	v_lshl_add_u64 v[6:7], v[6:7], 1, s[0:1]
	v_mul_hi_u32 v14, v1, s6
	v_lshl_add_u64 v[12:13], v[6:7], 0, v[10:11]
	v_mul_u32_u24_e32 v6, 20, v14
	v_sub_u32_e32 v1, v1, v6
	v_lshlrev_b32_e32 v10, 4, v1
	v_mad_u32_u24 v1, v14, s4, v10
	ds_read_b128 v[6:9], v1
	v_or_b32_e32 v1, s10, v14
	s_waitcnt lgkmcnt(1)
	global_store_dwordx4 v[12:13], v[2:5], off
	s_nop 1
	v_mad_i64_i32 v[2:3], s[2:3], v1, s5, 0
	v_lshl_add_u64 v[2:3], v[2:3], 1, s[0:1]
	v_lshl_add_u64 v[2:3], v[2:3], 0, v[10:11]
	v_or_b32_e32 v1, 0x800, v0
	s_waitcnt lgkmcnt(0)
	global_store_dwordx4 v[2:3], v[6:9], off
	s_nop 1
	v_mul_hi_u32 v6, v1, s6
	v_mul_u32_u24_e32 v2, 20, v6
	v_sub_u32_e32 v1, v1, v2
	v_lshlrev_b32_e32 v10, 4, v1
	v_mad_u32_u24 v1, v6, s4, v10
	ds_read_b128 v[2:5], v1
	v_or_b32_e32 v1, s10, v6
	v_mad_i64_i32 v[6:7], s[2:3], v1, s5, 0
	v_or_b32_e32 v1, 0xa00, v0
	v_lshl_add_u64 v[6:7], v[6:7], 1, s[0:1]
	v_mul_hi_u32 v14, v1, s6
	v_lshl_add_u64 v[12:13], v[6:7], 0, v[10:11]
	v_mul_u32_u24_e32 v6, 20, v14
	v_sub_u32_e32 v1, v1, v6
	v_lshlrev_b32_e32 v10, 4, v1
	v_mad_u32_u24 v1, v14, s4, v10
	ds_read_b128 v[6:9], v1
	v_or_b32_e32 v1, s10, v14
	s_waitcnt lgkmcnt(1)
	global_store_dwordx4 v[12:13], v[2:5], off
	s_nop 1
	v_mad_i64_i32 v[2:3], s[2:3], v1, s5, 0
	v_lshl_add_u64 v[2:3], v[2:3], 1, s[0:1]
	v_lshl_add_u64 v[2:3], v[2:3], 0, v[10:11]
	v_or_b32_e32 v1, 0xc00, v0
	s_waitcnt lgkmcnt(0)
	global_store_dwordx4 v[2:3], v[6:9], off
	s_nop 1
	v_mul_hi_u32 v6, v1, s6
	v_mul_u32_u24_e32 v2, 20, v6
	v_sub_u32_e32 v1, v1, v2
	v_lshlrev_b32_e32 v10, 4, v1
	v_mad_u32_u24 v1, v6, s4, v10
	ds_read_b128 v[2:5], v1
	v_or_b32_e32 v1, s10, v6
	v_mad_i64_i32 v[6:7], s[2:3], v1, s5, 0
	v_or_b32_e32 v1, 0xe00, v0
	v_lshl_add_u64 v[6:7], v[6:7], 1, s[0:1]
	v_mul_hi_u32 v14, v1, s6
	v_lshl_add_u64 v[12:13], v[6:7], 0, v[10:11]
	v_mul_u32_u24_e32 v6, 20, v14
	v_sub_u32_e32 v1, v1, v6
	v_lshlrev_b32_e32 v10, 4, v1
	v_mad_u32_u24 v1, v14, s4, v10
	ds_read_b128 v[6:9], v1
	v_add_u32_e32 v1, s10, v14
	s_waitcnt lgkmcnt(1)
	global_store_dwordx4 v[12:13], v[2:5], off
	s_nop 1
	v_mad_i64_i32 v[2:3], s[2:3], v1, s5, 0
	v_lshl_add_u64 v[2:3], v[2:3], 1, s[0:1]
	v_lshl_add_u64 v[2:3], v[2:3], 0, v[10:11]
	v_or_b32_e32 v1, 0x1000, v0
	s_waitcnt lgkmcnt(0)
	global_store_dwordx4 v[2:3], v[6:9], off
	v_or_b32_e32 v0, 0x1200, v0
	s_nop 0
	v_mul_hi_u32 v6, v1, s6
	v_mul_u32_u24_e32 v2, 20, v6
	v_sub_u32_e32 v1, v1, v2
	v_lshlrev_b32_e32 v10, 4, v1
	v_mad_u32_u24 v1, v6, s4, v10
	ds_read_b128 v[2:5], v1
	v_or_b32_e32 v1, s10, v6
	v_mad_i64_i32 v[6:7], s[2:3], v1, s5, 0
	v_lshl_add_u64 v[6:7], v[6:7], 1, s[0:1]
	v_mul_hi_u32 v1, v0, s6
	v_lshl_add_u64 v[12:13], v[6:7], 0, v[10:11]
	v_mul_u32_u24_e32 v6, 20, v1
	v_sub_u32_e32 v0, v0, v6
	v_lshlrev_b32_e32 v10, 4, v0
	v_mad_u32_u24 v0, v1, s4, v10
	ds_read_b128 v[6:9], v0
	v_add_u32_e32 v0, s10, v1
	v_mad_i64_i32 v[0:1], s[2:3], v0, s5, 0
	v_lshl_add_u64 v[0:1], v[0:1], 1, s[0:1]
	v_lshl_add_u64 v[0:1], v[0:1], 0, v[10:11]
	s_waitcnt lgkmcnt(1)
	global_store_dwordx4 v[12:13], v[2:5], off
	s_waitcnt lgkmcnt(0)
	global_store_dwordx4 v[0:1], v[6:9], off
	s_endpgm
	.p2alignl 8, 3212836864

_Z8gemm_f16ILi128ELi64ELi2ELi2ELi4ELi2ELi0EEvPKDF16_S1_Pviiii:
	s_load_dwordx4 s[4:7], s[0:1], 0x0
	s_load_dwordx2 s[8:9], s[0:1], 0x10
	s_and_b32 s3, s2, 7
	s_lshr_b32 s10, s2, 3
	s_lshl_b32 s3, s3, 1
	s_lshr_b32 s11, s10, 4
	s_add_i32 s3, s3, s11
	s_and_b32 s11, s10, 15
	s_lshl_b32 s10, s3, 7
	s_lshl_b32 s11, s11, 6
	v_lshrrev_b32_e32 v13, 3, v0
	v_and_b32_e32 v14, 7, v0
	v_bfe_u32 v15, v0, 4, 3
	v_xor_b32_e32 v14, v14, v15
	v_lshlrev_b32_e32 v14, 4, v14
	v_add_u32_e32 v15, s10, v13
	v_mul_u32_u24_e32 v15, 0xc00, v15
	v_add_u32_e32 v3, v15, v14
	v_add_u32_e32 v4, 0x18000, v3
	v_add_u32_e32 v5, 0x30000, v3
	v_add_u32_e32 v6, 0x48000, v3
	v_add_u32_e32 v15, s11, v13
	v_mul_u32_u24_e32 v15, 0xc00, v15
	v_add_u32_e32 v7, v15, v14
	v_add_u32_e32 v8, 0x18000, v7
	v_lshlrev_b32_e32 v13, 4, v0
	s_nop 0
	v_readfirstlane_b32 s20, v13
	v_and_b32_e32 v13, 15, v0
	v_bfe_u32 v14, v0, 4, 2
	v_bfe_u32 v15, v0, 1, 3
	v_xor_b32_e32 v14, v14, v15
	v_lshlrev_b32_e32 v14, 4, v14
	v_lshl_or_b32 v14, v13, 7, v14
	v_lshrrev_b32_e32 v13, 7, v0
	v_lshl_or_b32 v1, v13, 13, v14
	v_bfe_u32 v13, v0, 6, 1
	v_lshlrev_b32_e32 v13, 12, v13
	v_or_b32_e32 v13, 0x4000, v13
	v_or_b32_e32 v2, v13, v14
	s_waitcnt lgkmcnt(0)
	s_mov_b32 s14, s4
	s_mov_b32 s15, s5
	s_mov_b32 s16, s6
	s_mov_b32 s17, s7
	s_mov_b32 s21, s20
	s_mov_b32 m0, s21
	s_add_i32 s21, s21, 0x1000
	global_load_lds_dwordx4 v3, s[14:15]
	s_mov_b32 m0, s21
	s_add_i32 s21, s21, 0x1000
	global_load_lds_dwordx4 v4, s[14:15]
	s_mov_b32 m0, s21
	s_add_i32 s21, s21, 0x1000
	global_load_lds_dwordx4 v5, s[14:15]
	s_mov_b32 m0, s21
	s_add_i32 s21, s21, 0x1000
	global_load_lds_dwordx4 v6, s[14:15]
	s_mov_b32 m0, s21
	s_add_i32 s21, s21, 0x1000
	global_load_lds_dwordx4 v7, s[16:17]
	s_mov_b32 m0, s21
	s_add_i32 s21, s21, 0x1000
	global_load_lds_dwordx4 v8, s[16:17]
	s_add_u32 s14, s14, 0x80
	s_addc_u32 s15, s15, 0
	s_add_u32 s16, s16, 0x80
	s_addc_u32 s17, s17, 0
	s_mov_b32 m0, s21
	s_add_i32 s21, s21, 0x1000
	global_load_lds_dwordx4 v3, s[14:15]
	s_mov_b32 m0, s21
	s_add_i32 s21, s21, 0x1000
	global_load_lds_dwordx4 v4, s[14:15]
	s_mov_b32 m0, s21
	s_add_i32 s21, s21, 0x1000
	global_load_lds_dwordx4 v5, s[14:15]
	s_mov_b32 m0, s21
	s_add_i32 s21, s21, 0x1000
	global_load_lds_dwordx4 v6, s[14:15]
	s_mov_b32 m0, s21
	s_add_i32 s21, s21, 0x1000
	global_load_lds_dwordx4 v7, s[16:17]
	s_mov_b32 m0, s21
	s_add_i32 s21, s21, 0x1000
	global_load_lds_dwordx4 v8, s[16:17]
	s_add_u32 s14, s14, 0x80
	s_addc_u32 s15, s15, 0
	s_add_u32 s16, s16, 0x80
	s_addc_u32 s17, s17, 0
	s_mov_b32 m0, s21
	s_add_i32 s21, s21, 0x1000
	global_load_lds_dwordx4 v3, s[14:15]
	s_mov_b32 m0, s21
	s_add_i32 s21, s21, 0x1000
	global_load_lds_dwordx4 v4, s[14:15]
	s_mov_b32 m0, s21
	s_add_i32 s21, s21, 0x1000
	global_load_lds_dwordx4 v5, s[14:15]
	s_mov_b32 m0, s21
	s_add_i32 s21, s21, 0x1000
	global_load_lds_dwordx4 v6, s[14:15]
	s_mov_b32 m0, s21
	s_add_i32 s21, s21, 0x1000
	global_load_lds_dwordx4 v7, s[16:17]
	s_mov_b32 m0, s21
	s_add_i32 s21, s21, 0x1000
	global_load_lds_dwordx4 v8, s[16:17]
	s_add_u32 s14, s14, 0x80
	s_addc_u32 s15, s15, 0
	s_add_u32 s16, s16, 0x80
	s_addc_u32 s17, s17, 0
	s_mov_b32 m0, s21
	s_add_i32 s21, s21, 0x1000
	global_load_lds_dwordx4 v3, s[14:15]
	s_mov_b32 m0, s21
	s_add_i32 s21, s21, 0x1000
	global_load_lds_dwordx4 v4, s[14:15]
	s_mov_b32 m0, s21
	s_add_i32 s21, s21, 0x1000
	global_load_lds_dwordx4 v5, s[14:15]
	s_mov_b32 m0, s21
	s_add_i32 s21, s21, 0x1000
	global_load_lds_dwordx4 v6, s[14:15]
	s_mov_b32 m0, s21
	s_add_i32 s21, s21, 0x1000
	global_load_lds_dwordx4 v7, s[16:17]
	s_mov_b32 m0, s21
	s_add_i32 s21, s21, 0x1000
	global_load_lds_dwordx4 v8, s[16:17]
	v_accvgpr_write_b32 a0, 0
	v_accvgpr_write_b32 a1, 0
	v_accvgpr_write_b32 a2, 0
	v_accvgpr_write_b32 a3, 0
	v_accvgpr_write_b32 a4, 0
	v_accvgpr_write_b32 a5, 0
	v_accvgpr_write_b32 a6, 0
	v_accvgpr_write_b32 a7, 0
	v_accvgpr_write_b32 a8, 0
	v_accvgpr_write_b32 a9, 0
	v_accvgpr_write_b32 a10, 0
	v_accvgpr_write_b32 a11, 0
	v_accvgpr_write_b32 a12, 0
	v_accvgpr_write_b32 a13, 0
	v_accvgpr_write_b32 a14, 0
	v_accvgpr_write_b32 a15, 0
	v_accvgpr_write_b32 a16, 0
	v_accvgpr_write_b32 a17, 0
	v_accvgpr_write_b32 a18, 0
	v_accvgpr_write_b32 a19, 0
	v_accvgpr_write_b32 a20, 0
	v_accvgpr_write_b32 a21, 0
	v_accvgpr_write_b32 a22, 0
	v_accvgpr_write_b32 a23, 0
	v_accvgpr_write_b32 a24, 0
	v_accvgpr_write_b32 a25, 0
	v_accvgpr_write_b32 a26, 0
	v_accvgpr_write_b32 a27, 0
	v_accvgpr_write_b32 a28, 0
	v_accvgpr_write_b32 a29, 0
	v_accvgpr_write_b32 a30, 0
	v_accvgpr_write_b32 a31, 0
	s_mov_b32 s12, 0
	s_mov_b32 s13, 0
	v_mov_b32_e32 v9, v1
	v_mov_b32_e32 v11, v2
	v_xor_b32_e32 v10, 64, v1
	v_xor_b32_e32 v12, 64, v2
	s_waitcnt vmcnt(18)
	s_barrier
	ds_read_b128 v[16:19], v11
	ds_read_b128 v[24:27], v9
	ds_read_b128 v[20:23], v11 offset:2048
	ds_read_b128 v[28:31], v9 offset:2048
	ds_read_b128 v[32:35], v9 offset:4096
	ds_read_b128 v[36:39], v9 offset:6144
.Lg2_loop:
	ds_read_b128 v[40:43], v12
	ds_read_b128 v[48:51], v10
	ds_read_b128 v[44:47], v12 offset:2048
	ds_read_b128 v[52:55], v10 offset:2048
	ds_read_b128 v[56:59], v10 offset:4096
	ds_read_b128 v[60:63], v10 offset:6144
	s_add_i32 s22, s12, 4
	s_min_i32 s22, s22, 23
	s_lshl_b32 s22, s22, 7
	s_add_u32 s14, s4, s22
	s_addc_u32 s15, s5, 0
	s_add_u32 s16, s6, s22
	s_addc_u32 s17, s7, 0
	s_add_i32 s21, s13, s20
	s_add_i32 s23, s13, 0x6000
	s_cmp_lg_u32 s23, 0x18000
	s_cselect_b32 s23, s23, 0
	s_waitcnt lgkmcnt(6)
	v_mfma_f32_16x16x32_f16 a[0:3], v[16:19], v[24:27], a[0:3]
	v_mfma_f32_16x16x32_f16 a[4:7], v[20:23], v[24:27], a[4:7]
	v_add_u32_e32 v9, s23, v1
	v_mfma_f32_16x16x32_f16 a[8:11], v[16:19], v[28:31], a[8:11]
	v_mfma_f32_16x16x32_f16 a[12:15], v[20:23], v[28:31], a[12:15]
	v_add_u32_e32 v11, s23, v2
	v_mfma_f32_16x16x32_f16 a[16:19], v[16:19], v[32:35], a[16:19]
	v_mfma_f32_16x16x32_f16 a[20:23], v[20:23], v[32:35], a[20:23]
	v_xor_b32_e32 v10, 64, v9
	v_mfma_f32_16x16x32_f16 a[24:27], v[16:19], v[36:39], a[24:27]
	v_mfma_f32_16x16x32_f16 a[28:31], v[20:23], v[36:39], a[28:31]
	v_xor_b32_e32 v12, 64, v11
	s_waitcnt vmcnt(12)
	s_waitcnt lgkmcnt(0)
	s_barrier
	s_mov_b32 m0, s21
	s_add_i32 s21, s21, 0x1000
	global_load_lds_dwordx4 v3, s[14:15]
	s_mov_b32 m0, s21
	s_add_i32 s21, s21, 0x1000
	global_load_lds_dwordx4 v4, s[14:15]
	s_mov_b32 m0, s21
	s_add_i32 s21, s21, 0x1000
	global_load_lds_dwordx4 v5, s[14:15]
	s_mov_b32 m0, s21
	s_add_i32 s21, s21, 0x1000
	global_load_lds_dwordx4 v6, s[14:15]
	s_mov_b32 m0, s21
	s_add_i32 s21, s21, 0x1000
	global_load_lds_dwordx4 v7, s[16:17]
	s_mov_b32 m0, s21
	s_add_i32 s21, s21, 0x1000
	global_load_lds_dwordx4 v8, s[16:17]
	ds_read_b128 v[16:19], v11
	ds_read_b128 v[24:27], v9
	ds_read_b128 v[20:23], v11 offset:2048
	ds_read_b128 v[28:31], v9 offset:2048
	ds_read_b128 v[32:35], v9 offset:4096
	ds_read_b128 v[36:39], v9 offset:6144
	v_mfma_f32_16x16x32_f16 a[0:3], v[40:43], v[48:51], a[0:3]
	v_mfma_f32_16x16x32_f16 a[4:7], v[44:47], v[48:51], a[4:7]
	v_mfma_f32_16x16x32_f16 a[8:11], v[40:43], v[52:55], a[8:11]
	v_mfma_f32_16x16x32_f16 a[12:15], v[44:47], v[52:55], a[12:15]
	v_mfma_f32_16x16x32_f16 a[16:19], v[40:43], v[56:59], a[16:19]
	v_mfma_f32_16x16x32_f16 a[20:23], v[44:47], v[56:59], a[20:23]
	v_mfma_f32_16x16x32_f16 a[24:27], v[40:43], v[60:63], a[24:27]
	v_mfma_f32_16x16x32_f16 a[28:31], v[44:47], v[60:63], a[28:31]
	s_mov_b32 s13, s23
	s_add_i32 s12, s12, 1
	s_cmp_lt_u32 s12, 24
	s_cbranch_scc1 .Lg2_loop
	s_waitcnt vmcnt(0) lgkmcnt(0)
	v_and_b32_e32 v13, 15, v0
	v_lshrrev_b32_e32 v14, 7, v0
	v_lshl_add_u32 v13, v14, 6, v13
	v_add_u32_e32 v13, s10, v13
	v_bfe_u32 v14, v0, 6, 1
	v_bfe_u32 v15, v0, 4, 2
	v_lshlrev_b32_e32 v14, 5, v14
	v_lshl_add_u32 v14, v15, 2, v14
	v_add_u32_e32 v14, s11, v14
	v_lshlrev_b32_e32 v13, 10, v13
	v_add_u32_e32 v13, v13, v14
	v_lshlrev_b32_e32 v13, 2, v13
	v_add_u32_e32 v14, 0x10000, v13
	v_add_u32_e32 v15, 0x20000, v13
	v_add_u32_e32 v16, 0x30000, v13
	s_nop 7
	global_store_dwordx4 v13, a[0:3], s[8:9]
	global_store_dwordx4 v13, a[4:7], s[8:9] offset:64
	global_store_dwordx4 v14, a[8:11], s[8:9]
	global_store_dwordx4 v14, a[12:15], s[8:9] offset:64
	global_store_dwordx4 v15, a[16:19], s[8:9]
	global_store_dwordx4 v15, a[20:23], s[8:9] offset:64
	global_store_dwordx4 v16, a[24:27], s[8:9]
	global_store_dwordx4 v16, a[28:31], s[8:9] offset:64
	s_endpgm
	.p2alignl 8, 3212836864

	.amdhsa_kernel _Z8gemm_f16ILi128ELi64ELi2ELi2ELi4ELi2ELi0EEvPKDF16_S1_Pviiii
		.amdhsa_group_segment_fixed_size 98304
		.amdhsa_private_segment_fixed_size 0
		.amdhsa_kernarg_size 40
		.amdhsa_user_sgpr_count 2
		.amdhsa_user_sgpr_dispatch_ptr 0
		.amdhsa_user_sgpr_queue_ptr 0
		.amdhsa_user_sgpr_kernarg_segment_ptr 1
		.amdhsa_user_sgpr_dispatch_id 0
		.amdhsa_user_sgpr_kernarg_preload_length 0
		.amdhsa_user_sgpr_kernarg_preload_offset 0
		.amdhsa_user_sgpr_private_segment_size 0
		.amdhsa_uses_dynamic_stack 0
		.amdhsa_enable_private_segment 0
		.amdhsa_system_sgpr_workgroup_id_x 1
		.amdhsa_system_sgpr_workgroup_id_y 0
		.amdhsa_system_sgpr_workgroup_id_z 0
		.amdhsa_system_sgpr_workgroup_info 0
		.amdhsa_system_vgpr_workitem_id 0
		.amdhsa_next_free_vgpr 96
		.amdhsa_next_free_sgpr 32
		.amdhsa_accum_offset 64
		.amdhsa_reserve_vcc 0
		.amdhsa_float_round_mode_32 0
		.amdhsa_float_round_mode_16_64 0
		.amdhsa_float_denorm_mode_32 3
		.amdhsa_float_denorm_mode_16_64 3
		.amdhsa_dx10_clamp 1
		.amdhsa_ieee_mode 1
		.amdhsa_fp16_overflow 0
		.amdhsa_tg_split 0
		.amdhsa_exception_fp_ieee_invalid_op 0
		.amdhsa_exception_fp_denorm_src 0
		.amdhsa_exception_fp_ieee_div_zero 0
		.amdhsa_exception_fp_ieee_overflow 0
		.amdhsa_exception_fp_ieee_underflow 0
		.amdhsa_exception_fp_ieee_inexact 0
		.amdhsa_exception_int_div_zero 0
	.end_amdhsa_kernel

	.text
	.p2alignl 6, 3212836864
	.fill 256, 4, 3212836864
	.p2alignl 8, 3212836864

amdhsa.kernels:
  - .agpr_count:     0
    .args:
      - .offset:         0
        .size:           88
        .value_kind:     by_value
    .group_segment_fixed_size: 16640
    .kernarg_segment_align: 8
    .kernarg_segment_size: 88
    .language:       OpenCL C
    .language_version:
      - 2
      - 0
    .max_flat_workgroup_size: 256
    .name:           _Z15prologue_kernel7ProArgs
    .private_segment_fixed_size: 0
    .sgpr_count:     28
    .sgpr_spill_count: 0
    .symbol:         _Z15prologue_kernel7ProArgs.kd
    .uniform_work_group_size: 1
    .uses_dynamic_stack: false
    .vgpr_count:     54
    .vgpr_spill_count: 0
    .wavefront_size: 64
  - .agpr_count:     0
    .args:
      - .offset:         0
        .size:           96
        .value_kind:     by_value
    .group_segment_fixed_size: 149760
    .kernarg_segment_align: 8
    .kernarg_segment_size: 96
    .language:       OpenCL C
    .language_version:
      - 2
      - 0
    .max_flat_workgroup_size: 384
    .name:           _Z11prep_kernel8PrepArgs
    .private_segment_fixed_size: 0
    .sgpr_count:     41
    .sgpr_spill_count: 0
    .symbol:         _Z11prep_kernel8PrepArgs.kd
    .uniform_work_group_size: 1
    .uses_dynamic_stack: false
    .vgpr_count:     176
    .vgpr_spill_count: 0
    .wavefront_size: 64
  - .agpr_count:     0
    .args:
      - .actual_access:  read_only
        .address_space:  global
        .offset:         0
        .size:           8
        .value_kind:     global_buffer
      - .actual_access:  read_only
        .address_space:  global
        .offset:         8
        .size:           8
        .value_kind:     global_buffer
      - .actual_access:  read_only
        .address_space:  global
        .offset:         16
        .size:           8
        .value_kind:     global_buffer
      - .actual_access:  read_only
        .address_space:  global
        .offset:         24
        .size:           8
        .value_kind:     global_buffer
      - .actual_access:  write_only
        .address_space:  global
        .offset:         32
        .size:           8
        .value_kind:     global_buffer
      - .actual_access:  write_only
        .address_space:  global
        .offset:         40
        .size:           8
        .value_kind:     global_buffer
    .group_segment_fixed_size: 0
    .kernarg_segment_align: 8
    .kernarg_segment_size: 48
    .language:       OpenCL C
    .language_version:
      - 2
      - 0
    .max_flat_workgroup_size: 64
    .name:           _Z16rec_chunk_kernelPKDF16_PKfS2_S2_PfS3_
    .private_segment_fixed_size: 0
    .sgpr_count:     42
    .sgpr_spill_count: 0
    .symbol:         _Z16rec_chunk_kernelPKDF16_PKfS2_S2_PfS3_.kd
    .uniform_work_group_size: 1
    .uses_dynamic_stack: false
    .vgpr_count:     256
    .vgpr_spill_count: 0
    .wavefront_size: 64
  - .agpr_count:     0
    .args:
      - .actual_access:  read_only
        .address_space:  global
        .offset:         0
        .size:           8
        .value_kind:     global_buffer
      - .actual_access:  read_only
        .address_space:  global
        .offset:         8
        .size:           8
        .value_kind:     global_buffer
      - .actual_access:  read_only
        .address_space:  global
        .offset:         16
        .size:           8
        .value_kind:     global_buffer
      - .actual_access:  write_only
        .address_space:  global
        .offset:         24
        .size:           8
        .value_kind:     global_buffer
      - .actual_access:  read_only
        .address_space:  global
        .offset:         32
        .size:           8
        .value_kind:     global_buffer
      - .actual_access:  write_only
        .address_space:  global
        .offset:         40
        .size:           8
        .value_kind:     global_buffer
    .group_segment_fixed_size: 16640
    .kernarg_segment_align: 8
    .kernarg_segment_size: 48
    .language:       OpenCL C
    .language_version:
      - 2
      - 0
    .max_flat_workgroup_size: 256
    .name:           _Z16norm_gate_kernelPKfPKDF16_S0_PDF16_S0_S3_
    .private_segment_fixed_size: 0
    .sgpr_count:     20
    .sgpr_spill_count: 0
    .symbol:         _Z16norm_gate_kernelPKfPKDF16_S0_PDF16_S0_S3_.kd
    .uniform_work_group_size: 1
    .uses_dynamic_stack: false
    .vgpr_count:     63
    .vgpr_spill_count: 0
    .wavefront_size: 64
  - .agpr_count:     0
    .args:
      - .address_space:  global
        .offset:         0
        .size:           8
        .value_kind:     global_buffer
      - .address_space:  global
        .offset:         8
        .size:           8
        .value_kind:     global_buffer
      - .actual_access:  write_only
        .address_space:  global
        .offset:         16
        .size:           8
        .value_kind:     global_buffer
      - .offset:         24
        .size:           4
        .value_kind:     by_value
      - .offset:         28
        .size:           4
        .value_kind:     by_value
      - .offset:         32
        .size:           4
        .value_kind:     by_value
      - .offset:         36
        .size:           4
        .value_kind:     by_value
    .group_segment_fixed_size: 106496
    .kernarg_segment_align: 8
    .kernarg_segment_size: 40
    .language:       OpenCL C
    .language_version:
      - 2
      - 0
    .max_flat_workgroup_size: 512
    .name:           _Z8gemm_f16ILi256ELi160ELi4ELi2ELi2ELi1ELi1EEvPKDF16_S1_Pviiii
    .private_segment_fixed_size: 0
    .sgpr_count:     22
    .sgpr_spill_count: 0
    .symbol:         _Z8gemm_f16ILi256ELi160ELi4ELi2ELi2ELi1ELi1EEvPKDF16_S1_Pviiii.kd
    .uniform_work_group_size: 1
    .uses_dynamic_stack: false
    .vgpr_count:     140
    .vgpr_spill_count: 0
    .wavefront_size: 64
  - .agpr_count:     32
    .args:
      - .address_space:  global
        .offset:         0
        .size:           8
        .value_kind:     global_buffer
      - .address_space:  global
        .offset:         8
        .size:           8
        .value_kind:     global_buffer
      - .actual_access:  write_only
        .address_space:  global
        .offset:         16
        .size:           8
        .value_kind:     global_buffer
      - .offset:         24
        .size:           4
        .value_kind:     by_value
      - .offset:         28
        .size:           4
        .value_kind:     by_value
      - .offset:         32
        .size:           4
        .value_kind:     by_value
      - .offset:         36
        .size:           4
        .value_kind:     by_value
    .group_segment_fixed_size: 98304
    .kernarg_segment_align: 8
    .kernarg_segment_size: 40
    .language:       OpenCL C
    .language_version:
      - 2
      - 0
    .max_flat_workgroup_size: 256
    .name:           _Z8gemm_f16ILi128ELi64ELi2ELi2ELi4ELi2ELi0EEvPKDF16_S1_Pviiii
    .private_segment_fixed_size: 0
    .sgpr_count:     38
    .sgpr_spill_count: 0
    .symbol:         _Z8gemm_f16ILi128ELi64ELi2ELi2ELi4ELi2ELi0EEvPKDF16_S1_Pviiii.kd
    .uniform_work_group_size: 1
    .uses_dynamic_stack: false
    .vgpr_count:     96
    .vgpr_spill_count: 0
    .wavefront_size: 64
